# P1: converter workgroups per XCD 12 -> 11 (converter loop is faster since v52), on top of v63
# speedup vs baseline: 1.0151x; 1.0151x over previous
; #define F8_LD(v, s_, d_, ok) do { ok = it < NEXP; if (ok) { f8_item(p, it, s_, d_); f8_tile_load(s_, v, lane); } it += stride; } while (0)
; __device__ __forceinline__ void f8_item(const Params& p, int it, const float*& src, unsigned char*& dst) {
;     const int which = it >> 15, r = it & 32767, e = r >> 10, q = r & 1023, kb = q >> 6, nb = q & 63;
;     if (which == 2) { src = p.w_down + (size_t)e * FF * D + (size_t)(kb * 128) * D + nb * 32; dst = p.ws + WS_WD + ((size_t)e * D + nb * 32) * 2048 + kb * 128; }
;     else { const int f0 = nb * 32, drow = (f0 >> 7) * 256 + which * 128 + (f0 & 127);
;         src = (which == 0 ? p.w_gate : p.w_up) + (size_t)e * D * FF + (size_t)(kb * 128) * FF + f0; dst = p.ws + WS_WGU + ((size_t)e * 4096 + drow) * 2048 + kb * 128; }
; }
; __device__ __forceinline__ void convert_experts(const Params& p, int first, int stride, int lane) {
;     constexpr int NEXP = 3 * NE * 1024;
;     f32x4 va[16], vb[16], vc[16]; const float* sa; unsigned char* da; const float* sb; unsigned char* db; const float* sc; unsigned char* dc;
;     int it = first; bool oka, okb, okc;
;     ...
;     F8_LD(va, sa, da, oka); F8_LD(vb, sb, db, okb); F8_LD(vc, sc, dc, okc);
; __global__ void __launch_bounds__(NTHREADS, 2) hymba_fwd(Params p) {
;     ...
;         const int ncw = (G < 8 * NCV) ? G : 8 * NCV;
;         if (cid < ncw) convert_experts(p, cid * NWAVES + wave, ncw * NWAVES, lane);
.LBB0_146:
	s_load_dwordx16 s[12:27], s[0:1], 0x80
	s_cmp_lt_i32 s48, 2
	s_cselect_b64 s[4:5], -1, 0
	s_and_b64 s[0:1], s[4:5], s[10:11]
	s_andn2_b64 vcc, exec, s[0:1]
	s_waitcnt lgkmcnt(0)
	v_writelane_b32 v255, s12, 29
	s_mov_b32 s0, s90
	s_nop 0
	v_writelane_b32 v255, s13, 30
	v_writelane_b32 v255, s14, 31
	v_writelane_b32 v255, s15, 32
	v_writelane_b32 v255, s16, 33
	v_writelane_b32 v255, s17, 34
	v_writelane_b32 v255, s18, 35
	v_writelane_b32 v255, s19, 36
	v_writelane_b32 v255, s20, 37
	v_writelane_b32 v255, s21, 38
	v_writelane_b32 v255, s22, 39
	v_writelane_b32 v255, s23, 40
	v_writelane_b32 v255, s24, 41
	v_writelane_b32 v255, s25, 42
	v_writelane_b32 v255, s26, 43
	v_writelane_b32 v255, s27, 44
	v_writelane_b32 v255, s0, 45
	s_nop 1
	v_writelane_b32 v255, s1, 46
	s_mov_b32 s0, s68
	v_writelane_b32 v255, s0, 47
	s_nop 1
	v_writelane_b32 v255, s1, 48
	s_cbranch_vccnz .LBB0_224
	s_min_i32 s27, s96, 0x58
	v_readlane_b32 s0, v255, 28
	s_cmp_ge_i32 s0, s27
	s_cbranch_scc1 .LBB0_192
	v_readlane_b32 s0, v255, 28
	s_lshl_b32 s0, s0, 3
	v_readlane_b32 s6, v255, 22
	s_add_i32 s2, s0, s6
	s_cmp_lt_i32 s2, 0x18000
	s_cselect_b64 s[14:15], -1, 0
	s_cmp_gt_i32 s2, 0x17fff
	v_readlane_b32 s7, v255, 23
	s_cbranch_scc1 .LBB0_151
	s_ashr_i32 s0, s2, 15
	s_bfe_u32 s10, s2, 0x5000a
	s_bfe_u32 s12, s2, 0x40006
	s_and_b32 s11, s2, 63
	s_cmp_lg_u32 s0, 2
	s_cbranch_scc0 .LBB0_152
	s_lshl_b32 s6, s11, 6
	s_lshl_b32 s1, s11, 5
	s_and_b32 s6, s6, 0xf00
	s_lshl_b32 s0, s0, 7
	s_add_i32 s6, s6, s0
	s_and_b32 s0, s1, 0x60
	s_or_b32 s0, s6, s0
	v_readlane_b32 s52, v255, 29
	s_cmpk_lt_u32 s2, 0x8000
	v_readlane_b32 s54, v255, 31
	v_readlane_b32 s55, v255, 32
	v_readlane_b32 s58, v255, 35
	v_readlane_b32 s59, v255, 36
	s_cselect_b32 s1, s55, s59
	s_cselect_b32 s6, s54, s58
	s_lshl_b32 s7, s10, 24
	s_add_u32 s6, s6, s7
	s_addc_u32 s1, s1, 0
	s_lshl_b32 s8, s12, 7
	s_lshl_b32 s7, s12, 20
	s_add_u32 s6, s6, s7
	s_addc_u32 s1, s1, 0
	s_lshl_b32 s7, s11, 7
	s_add_u32 s6, s6, s7
	s_addc_u32 s7, s1, 0
	s_ashr_i32 s1, s0, 31
	s_lshl_b32 s9, s10, 23
	s_lshl_b64 s[0:1], s[0:1], 11
	s_add_u32 s9, s88, s9
	s_addc_u32 s13, s89, 0
	s_add_u32 s0, s9, s0
	s_addc_u32 s1, s13, s1
	s_add_u32 s0, s0, s8
	s_addc_u32 s1, s1, 0
	s_add_u32 s0, s0, 0x1000000
	v_readlane_b32 s53, v255, 30
	v_readlane_b32 s56, v255, 33
	v_readlane_b32 s57, v255, 34
	v_readlane_b32 s60, v255, 37
	v_readlane_b32 s61, v255, 38
	v_readlane_b32 s62, v255, 39
	v_readlane_b32 s63, v255, 40
	v_readlane_b32 s64, v255, 41
	v_readlane_b32 s65, v255, 42
	v_readlane_b32 s66, v255, 43
	v_readlane_b32 s67, v255, 44
	s_addc_u32 s1, s1, 0
	s_cbranch_execz .LBB0_153
	s_branch .LBB0_154
